# E25: E24 + back-edge rotation (guide 7.11) of the NSA sel-far and win-far tile loops: loop-carried copies, next-tile scalar chain and LDS-DMA address math moved in front of the tile-end barrier; post-
# speedup vs baseline: 1.0061x; 1.0061x over previous
.LBB0_697:
	v_sub_f32_e32 v0, v5, v134
	v_fmamk_f32 v5, v98, 0x3fb8aa3b, v0
	v_exp_f32_e32 v98, v5
	v_fmamk_f32 v5, v99, 0x3fb8aa3b, v0
	v_exp_f32_e32 v99, v5
	v_fmamk_f32 v5, v100, 0x3fb8aa3b, v0
	v_exp_f32_e32 v100, v5
	v_fmamk_f32 v5, v101, 0x3fb8aa3b, v0
	v_exp_f32_e32 v101, v5
	v_fmamk_f32 v94, v94, 0x3fb8aa3b, v0
	v_add_f32_e32 v5, 0, v98
	v_exp_f32_e32 v94, v94
	v_fmamk_f32 v95, v95, 0x3fb8aa3b, v0
	v_add_f32_e32 v5, v99, v5
	v_exp_f32_e32 v95, v95
	v_fmamk_f32 v96, v96, 0x3fb8aa3b, v0
	v_add_f32_e32 v5, v100, v5
	v_exp_f32_e32 v96, v96
	v_fmamk_f32 v97, v97, 0x3fb8aa3b, v0
	v_add_f32_e32 v5, v101, v5
	v_exp_f32_e32 v97, v97
	v_fmamk_f32 v90, v90, 0x3fb8aa3b, v0
	v_add_f32_e32 v5, v94, v5
	v_exp_f32_e32 v90, v90
	v_fmamk_f32 v91, v91, 0x3fb8aa3b, v0
	v_add_f32_e32 v5, v95, v5
	v_exp_f32_e32 v91, v91
	v_fmamk_f32 v92, v92, 0x3fb8aa3b, v0
	v_add_f32_e32 v5, v96, v5
	v_exp_f32_e32 v92, v92
	v_fmamk_f32 v93, v93, 0x3fb8aa3b, v0
	v_add_f32_e32 v5, v97, v5
	v_exp_f32_e32 v93, v93
	v_fmamk_f32 v86, v86, 0x3fb8aa3b, v0
	v_add_f32_e32 v5, v90, v5
	v_exp_f32_e32 v198, v86
	v_fmamk_f32 v86, v87, 0x3fb8aa3b, v0
	v_add_f32_e32 v5, v91, v5
	v_exp_f32_e32 v199, v86
	v_fmamk_f32 v86, v88, 0x3fb8aa3b, v0
	v_add_f32_e32 v5, v92, v5
	v_exp_f32_e32 v200, v86
	v_fmac_f32_e32 v0, 0x3fb8aa3b, v89
	v_add_f32_e32 v5, v93, v5
	v_exp_f32_e32 v0, v0
	v_add_f32_e32 v5, v198, v5
	v_add_f32_e32 v5, v199, v5
	v_add_f32_e32 v5, v200, v5
	v_add_f32_e32 v5, v0, v5
	v_fmac_f32_e32 v5, v136, v4
	v_sub_f32_e32 v4, v137, v125
	v_fmamk_f32 v82, v82, 0x3fb8aa3b, v4
	v_exp_f32_e32 v82, v82
	v_fmamk_f32 v83, v83, 0x3fb8aa3b, v4
	v_exp_f32_e32 v83, v83
	v_fmamk_f32 v84, v84, 0x3fb8aa3b, v4
	v_exp_f32_e32 v84, v84
	v_fmamk_f32 v85, v85, 0x3fb8aa3b, v4
	v_exp_f32_e32 v85, v85
	v_fmamk_f32 v78, v78, 0x3fb8aa3b, v4
	v_add_f32_e32 v86, 0, v82
	v_exp_f32_e32 v87, v78
	v_fmamk_f32 v78, v79, 0x3fb8aa3b, v4
	v_add_f32_e32 v86, v83, v86
	v_exp_f32_e32 v88, v78
	v_fmamk_f32 v78, v80, 0x3fb8aa3b, v4
	v_add_f32_e32 v86, v84, v86
	v_exp_f32_e32 v89, v78
	v_fmamk_f32 v78, v81, 0x3fb8aa3b, v4
	v_add_f32_e32 v86, v85, v86
	v_exp_f32_e32 v81, v78
	v_fmamk_f32 v74, v74, 0x3fb8aa3b, v4
	v_add_f32_e32 v78, v87, v86
	v_exp_f32_e32 v136, v74
	v_fmamk_f32 v74, v75, 0x3fb8aa3b, v4
	v_add_f32_e32 v78, v88, v78
	v_exp_f32_e32 v137, v74
	v_fmamk_f32 v74, v76, 0x3fb8aa3b, v4
	v_add_f32_e32 v78, v89, v78
	v_exp_f32_e32 v201, v74
	v_fmamk_f32 v74, v77, 0x3fb8aa3b, v4
	v_add_f32_e32 v78, v81, v78
	v_exp_f32_e32 v202, v74
	v_fmamk_f32 v70, v70, 0x3fb8aa3b, v4
	v_add_f32_e32 v74, v136, v78
	v_exp_f32_e32 v203, v70
	v_fmamk_f32 v70, v71, 0x3fb8aa3b, v4
	v_add_f32_e32 v74, v137, v74
	v_exp_f32_e32 v204, v70
	v_fmamk_f32 v70, v72, 0x3fb8aa3b, v4
	v_add_f32_e32 v74, v201, v74
	v_exp_f32_e32 v205, v70
	v_fmac_f32_e32 v4, 0x3fb8aa3b, v73
	v_add_f32_e32 v74, v202, v74
	v_exp_f32_e32 v4, v4
	v_add_f32_e32 v70, v203, v74
	s_cmp_eq_u32 s83, 0
	v_add_f32_e32 v70, v204, v70
	v_add_f32_e32 v70, v205, v70
	s_cselect_b32 s0, 0x8000, s79
	v_add_f32_e32 v133, v4, v70
	s_add_i32 s0, s0, 0
	v_fmac_f32_e32 v133, v135, v2
	v_add_u32_e32 v2, s0, v142
	ds_read_b128 v[70:73], v2
	ds_read_b128 v[74:77], v2 offset:2048
	v_cvt_pk_bf16_f32 v78, v82, v83
	v_cvt_pk_bf16_f32 v79, v84, v85
	ds_read_b128 v[82:85], v2 offset:4096
	v_cvt_pk_bf16_f32 v80, v87, v88
	v_cvt_pk_bf16_f32 v81, v89, v81
	v_cvt_pk_bf16_f32 v86, v98, v99
	v_cvt_pk_bf16_f32 v87, v100, v101
	v_cvt_pk_bf16_f32 v88, v94, v95
	v_cvt_pk_bf16_f32 v89, v96, v97
	s_waitcnt lgkmcnt(2)
	v_mfma_f32_16x16x32_bf16 v[66:69], v[70:73], v[78:81], v[66:69]
	v_mfma_f32_16x16x32_bf16 v[34:37], v[70:73], v[86:89], v[34:37]
	ds_read_b128 v[70:73], v2 offset:6144
	s_waitcnt lgkmcnt(2)
	v_mfma_f32_16x16x32_bf16 v[62:65], v[74:77], v[78:81], v[62:65]
	v_mfma_f32_16x16x32_bf16 v[30:33], v[74:77], v[86:89], v[30:33]
	ds_read_b128 v[74:77], v2 offset:8192
	s_waitcnt lgkmcnt(2)
	v_mfma_f32_16x16x32_bf16 v[58:61], v[82:85], v[78:81], v[58:61]
	v_mfma_f32_16x16x32_bf16 v[26:29], v[82:85], v[86:89], v[26:29]
	ds_read_b128 v[82:85], v2 offset:10240
	s_waitcnt lgkmcnt(2)
	v_mfma_f32_16x16x32_bf16 v[54:57], v[70:73], v[78:81], v[54:57]
	v_mfma_f32_16x16x32_bf16 v[22:25], v[70:73], v[86:89], v[22:25]
	ds_read_b128 v[70:73], v2 offset:12288
	s_waitcnt lgkmcnt(2)
	v_mfma_f32_16x16x32_bf16 v[50:53], v[74:77], v[78:81], v[50:53]
	v_mfma_f32_16x16x32_bf16 v[18:21], v[74:77], v[86:89], v[18:21]
	ds_read_b128 v[74:77], v2 offset:14336
	v_add_u32_e32 v2, s0, v146
	s_waitcnt lgkmcnt(2)
	v_mfma_f32_16x16x32_bf16 v[46:49], v[82:85], v[78:81], v[46:49]
	v_mfma_f32_16x16x32_bf16 v[14:17], v[82:85], v[86:89], v[14:17]
	ds_read_b128 v[82:85], v2
	s_waitcnt lgkmcnt(2)
	v_mfma_f32_16x16x32_bf16 v[42:45], v[70:73], v[78:81], v[42:45]
	v_mfma_f32_16x16x32_bf16 v[10:13], v[70:73], v[86:89], v[10:13]
	ds_read_b128 v[70:73], v2 offset:2048
	s_waitcnt lgkmcnt(2)
	v_mfma_f32_16x16x32_bf16 v[38:41], v[74:77], v[78:81], v[38:41]
	v_cvt_pk_bf16_f32 v78, v90, v91
	v_cvt_pk_bf16_f32 v79, v92, v93
	v_cvt_pk_bf16_f32 v80, v198, v199
	v_mfma_f32_16x16x32_bf16 v[6:9], v[74:77], v[86:89], v[6:9]
	ds_read_b128 v[86:89], v2 offset:4096
	v_cvt_pk_bf16_f32 v74, v136, v137
	v_cvt_pk_bf16_f32 v75, v201, v202
	v_cvt_pk_bf16_f32 v76, v203, v204
	v_cvt_pk_bf16_f32 v77, v205, v4
	v_cvt_pk_bf16_f32 v81, v200, v0
	s_nop 0
	s_waitcnt lgkmcnt(2)
	v_mfma_f32_16x16x32_bf16 v[66:69], v[82:85], v[74:77], v[66:69]
	v_mfma_f32_16x16x32_bf16 v[34:37], v[82:85], v[78:81], v[34:37]
	ds_read_b128 v[82:85], v2 offset:6144
	s_waitcnt lgkmcnt(2)
	v_mfma_f32_16x16x32_bf16 v[62:65], v[70:73], v[74:77], v[62:65]
	v_mfma_f32_16x16x32_bf16 v[30:33], v[70:73], v[78:81], v[30:33]
	ds_read_b128 v[70:73], v2 offset:8192
	s_waitcnt lgkmcnt(2)
	v_mfma_f32_16x16x32_bf16 v[58:61], v[86:89], v[74:77], v[58:61]
	v_mfma_f32_16x16x32_bf16 v[26:29], v[86:89], v[78:81], v[26:29]
	ds_read_b128 v[86:89], v2 offset:10240
	s_waitcnt lgkmcnt(2)
	v_mfma_f32_16x16x32_bf16 v[54:57], v[82:85], v[74:77], v[54:57]
	v_mfma_f32_16x16x32_bf16 v[22:25], v[82:85], v[78:81], v[22:25]
	ds_read_b128 v[82:85], v2 offset:12288
	s_waitcnt lgkmcnt(2)
	v_mfma_f32_16x16x32_bf16 v[50:53], v[70:73], v[74:77], v[50:53]
	v_mfma_f32_16x16x32_bf16 v[18:21], v[70:73], v[78:81], v[18:21]
	ds_read_b128 v[70:73], v2 offset:14336
	s_waitcnt lgkmcnt(2)
	v_mfma_f32_16x16x32_bf16 v[46:49], v[86:89], v[74:77], v[46:49]
	v_mfma_f32_16x16x32_bf16 v[14:17], v[86:89], v[78:81], v[14:17]
	s_waitcnt lgkmcnt(1)
	v_mfma_f32_16x16x32_bf16 v[42:45], v[82:85], v[74:77], v[42:45]
	v_mfma_f32_16x16x32_bf16 v[10:13], v[82:85], v[78:81], v[10:13]
	s_waitcnt lgkmcnt(0)
	v_mfma_f32_16x16x32_bf16 v[38:41], v[70:73], v[74:77], v[38:41]
	s_waitcnt vmcnt(0)
	s_add_i32 s33, s33, 1
	s_add_i32 s0, s8, s33
	v_mfma_f32_16x16x32_bf16 v[6:9], v[70:73], v[78:81], v[6:9]
	s_cmp_eq_u32 s0, 1
	s_cbranch_scc1 .Lx687_exit
	v_mov_b32_e32 v136, v5
	v_mov_b32_e32 v135, v133
	v_mov_b32_e32 v133, v125
	v_mov_b32_e32 v4, v134
	s_add_i32 s0, s33, -1
	s_and_b32 s83, s0, 1
	s_add_i32 s3, s3, 1
	s_lshl_b32 s0, s83, 14
	s_add_i32 s0, s0, 0
	v_add_u32_e32 v0, s0, v140
	s_add_i32 s1, s37, s33
	s_add_i32 s1, s1, -1
	s_mov_b32 s32, 0
	s_add_i32 s98, s33, -1
	s_cmp_ge_u32 s98, s86
	s_cbranch_scc1 .Lx687_pd
	s_cmp_ge_i32 s33, s42
	s_mov_b64 s[98:99], -1
	s_cbranch_scc0 .Lx687_a
	s_add_i32 s98, s8, s33
	s_cmp_ge_i32 s98, s43
	s_cselect_b32 s99, s82, 0
	s_add_i32 s22, s98, s99
	s_mov_b64 s[98:99], 0

.Lx687_b:
	s_lshl_b32 s98, s22, 6
	s_lshl_b32 s22, s22, 13
	s_ashr_i32 s23, s22, 31
	s_lshl_b64 s[22:23], s[22:23], 1
	s_add_u32 s22, s46, s22
	s_addc_u32 s23, s47, s23
	s_cmp_eq_u32 s83, 0
	s_cselect_b32 s99, 0x4000, 0
	s_cselect_b32 s30, s79, 0x8000
	s_add_i32 s99, s28, s99
	v_lshl_add_u64 v[240:241], s[22:23], 0, v[102:103]
	s_mov_b32 s100, s99
	s_ashr_i32 s99, s98, 31
	s_lshl_b64 s[98:99], s[98:99], 1
	s_add_u32 s98, s44, s98
	v_lshl_add_u64 v[242:243], s[22:23], 0, v[108:109]
	s_addc_u32 s99, s45, s99
	s_add_i32 s22, s28, s30
	v_lshl_add_u64 v[244:245], s[98:99], 0, v[106:107]
	s_mov_b32 s101, s22
	v_lshl_add_u64 v[246:247], s[98:99], 0, v[112:113]
	s_mov_b32 s32, 1
.Lx687_pd:
	s_waitcnt vmcnt(0)
	s_barrier
	ds_read_b128 v[70:73], v0
	ds_read_b128 v[74:77], v0 offset:4096
	ds_read_b128 v[78:81], v197
	ds_read_b128 v[82:85], v197 offset:4096
	ds_read_b128 v[86:89], v0 offset:8192
	ds_read_b128 v[94:97], v0 offset:12288
	s_cmp_eq_u32 s32, 0
	s_cbranch_scc1 .Lr687_skip
	s_mov_b32 m0, s100
	s_nop 0
	global_load_lds_dwordx4 v[240:241], off
	s_add_i32 m0, s100, 0x400
	s_nop 0
	global_load_lds_dwordx4 v[242:243], off
	s_mov_b32 m0, s101
	s_nop 0
	global_load_lds_dwordx4 v[244:245], off
	s_add_i32 m0, s101, 0x400
	s_nop 0
	global_load_lds_dwordx4 v[246:247], off
	s_branch .Lr687_skip
.Lx687_exit:
	s_waitcnt vmcnt(0)
	s_barrier
	s_branch .LBB0_700

.LBB0_700:
	s_lshl_b32 s8, s36, 19
	s_cmp_gt_i32 s82, s86
	s_cbranch_scc1 .LBB0_781
	s_sub_i32 s36, s2, s43
	s_sub_i32 s84, 0, s42
	s_cmp_ge_i32 s82, s42
	s_mov_b64 s[0:1], -1
	s_cbranch_scc0 .LBB0_704
	s_branch .LBB0_703
	s_nop 0
	s_nop 0
	s_nop 0
	s_nop 0
	s_nop 0
	s_nop 0
	s_nop 0
	s_nop 0
	s_nop 0
	s_nop 0
	s_nop 0
	s_nop 0
	s_nop 0
	s_nop 0
	s_nop 0
	s_nop 0
	s_nop 0
	s_nop 0
	s_nop 0
	s_nop 0
	s_nop 0
	s_nop 0
	s_nop 0
	s_nop 0
	s_nop 0
	s_nop 0
	s_nop 0
	s_nop 0
	s_nop 0
	s_nop 0
	s_nop 0
	s_nop 0
	s_nop 0
	s_nop 0

.LBB0_789:
	s_lshl_b32 s2, s8, 1
	v_readlane_b32 s3, v253, 24
	s_add_u32 s8, s3, s2
	v_readlane_b32 s3, v253, 26
	s_addc_u32 s44, s3, 0
	v_readlane_b32 s3, v253, 28
	s_add_u32 s45, s3, s2
	v_readlane_b32 s2, v253, 30
	s_addc_u32 s46, s2, 0
	s_lshl_b32 s2, s22, 6
	s_lshl_b32 s22, s22, 13
	s_ashr_i32 s23, s22, 31
	s_lshl_b64 s[22:23], s[22:23], 1
	s_add_u32 s22, s8, s22
	s_addc_u32 s23, s44, s23
	s_ashr_i32 s3, s2, 31
	s_lshl_b64 s[2:3], s[2:3], 1
	s_mov_b32 m0, s28
	v_lshl_add_u64 v[4:5], s[22:23], 0, v[102:103]
	s_add_u32 s2, s45, s2
	global_load_lds_dwordx4 v[4:5], off
	v_lshl_add_u64 v[4:5], s[22:23], 0, v[108:109]
	s_mov_b32 m0, s81
	s_addc_u32 s3, s46, s3
	global_load_lds_dwordx4 v[4:5], off
	v_lshl_add_u64 v[4:5], s[2:3], 0, v[106:107]
	s_mov_b32 m0, s77
	s_andn2_b64 vcc, exec, s[0:1]
	global_load_lds_dwordx4 v[4:5], off
	v_lshl_add_u64 v[4:5], s[2:3], 0, v[112:113]
	s_mov_b32 m0, s78
	s_nop 0
	global_load_lds_dwordx4 v[4:5], off
	s_waitcnt vmcnt(0)
	s_waitcnt vmcnt(0) lgkmcnt(0)
	s_barrier
	s_cbranch_vccnz .LBB0_807
	v_readlane_b32 s0, v253, 38
	s_add_i32 s0, s0, s33
	v_mov_b32_e32 v4, v3
	v_mov_b32_e32 v5, v3
	s_sub_i32 s0, s0, s42
	v_mov_b32_e32 v2, v3
	v_mov_b64_e32 v[8:9], v[4:5]
	v_mov_b64_e32 v[12:13], v[4:5]
	v_mov_b64_e32 v[16:17], v[4:5]
	v_mov_b64_e32 v[20:21], v[4:5]
	v_mov_b64_e32 v[24:25], v[4:5]
	v_mov_b64_e32 v[28:29], v[4:5]
	v_mov_b64_e32 v[32:33], v[4:5]
	v_mov_b64_e32 v[36:37], v[4:5]
	v_mov_b64_e32 v[40:41], v[4:5]
	v_mov_b64_e32 v[44:45], v[4:5]
	v_mov_b64_e32 v[48:49], v[4:5]
	v_mov_b64_e32 v[52:53], v[4:5]
	v_mov_b64_e32 v[56:57], v[4:5]
	v_mov_b64_e32 v[60:61], v[4:5]
	v_mov_b64_e32 v[64:65], v[4:5]
	v_mov_b64_e32 v[68:69], v[4:5]
	s_sub_i32 s2, s0, s36
	s_mov_b32 s22, 0
	s_sub_i32 s3, 0, s42
	v_mov_b32_e32 v137, 0xf149f2ca
	v_mov_b32_e32 v136, 0
	v_mov_b32_e32 v135, 0
	v_mov_b64_e32 v[6:7], v[2:3]
	v_mov_b64_e32 v[10:11], v[2:3]
	v_mov_b64_e32 v[14:15], v[2:3]
	v_mov_b64_e32 v[18:19], v[2:3]
	v_mov_b64_e32 v[22:23], v[2:3]
	v_mov_b64_e32 v[26:27], v[2:3]
	v_mov_b64_e32 v[30:31], v[2:3]
	v_mov_b64_e32 v[34:35], v[2:3]
	v_mov_b64_e32 v[38:39], v[2:3]
	v_mov_b64_e32 v[42:43], v[2:3]
	v_mov_b64_e32 v[46:47], v[2:3]
	v_mov_b64_e32 v[50:51], v[2:3]
	v_mov_b64_e32 v[54:55], v[2:3]
	v_mov_b64_e32 v[58:59], v[2:3]
	v_mov_b64_e32 v[62:63], v[2:3]
	v_mov_b64_e32 v[66:67], v[2:3]
	v_mov_b32_e32 v4, 0xf149f2ca
	s_and_b32 s81, s22, 1
	s_add_i32 s47, s22, 1
	s_cmp_ge_i32 s22, s93
	s_cbranch_scc1 .LBB0_801
	s_branch .LBB0_792
	s_nop 0
	s_nop 0
	s_nop 0
	s_nop 0
.LBB0_792:
	s_cmp_lt_i32 s47, s42
	s_mov_b64 s[0:1], -1
	s_cbranch_scc1 .LBB0_798
	s_add_i32 s0, s3, s22
	s_add_i32 s0, s0, 1
	s_cmp_lt_i32 s0, s43
	s_mov_b64 s[0:1], -1
	s_cbranch_scc1 .LBB0_795
	s_add_i32 s23, s2, s22
	s_mov_b64 s[0:1], 0

.Lx791_body:
	s_waitcnt lgkmcnt(0)
	v_mfma_f32_16x16x32_bf16 v[90:93], v[70:73], v[78:81], 0
	v_mfma_f32_16x16x32_bf16 v[70:73], v[70:73], v[82:85], 0
	v_add_u32_e32 v0, s0, v143
	ds_read_b128 v[198:201], v0
	ds_read_b128 v[202:205], v197 offset:1024
	ds_read_b128 v[206:209], v197 offset:5120
	v_mfma_f32_16x16x32_bf16 v[98:101], v[74:77], v[78:81], 0
	v_mfma_f32_16x16x32_bf16 v[74:77], v[74:77], v[82:85], 0
	v_mfma_f32_16x16x32_bf16 v[210:213], v[86:89], v[78:81], 0
	ds_read_b128 v[214:217], v0 offset:4096
	v_mfma_f32_16x16x32_bf16 v[86:89], v[86:89], v[82:85], 0
	v_mfma_f32_16x16x32_bf16 v[78:81], v[94:97], v[78:81], 0
	v_mfma_f32_16x16x32_bf16 v[82:85], v[94:97], v[82:85], 0
	ds_read_b128 v[94:97], v0 offset:8192
	s_waitcnt lgkmcnt(3)
	v_mfma_f32_16x16x32_bf16 v[90:93], v[198:201], v[202:205], v[90:93]
	s_waitcnt lgkmcnt(2)
	v_mfma_f32_16x16x32_bf16 v[70:73], v[198:201], v[206:209], v[70:73]
	ds_read_b128 v[198:201], v0 offset:12288
	v_add_u32_e32 v0, s0, v144
	s_waitcnt lgkmcnt(2)
	v_mfma_f32_16x16x32_bf16 v[98:101], v[214:217], v[202:205], v[98:101]
	v_mfma_f32_16x16x32_bf16 v[74:77], v[214:217], v[206:209], v[74:77]
	ds_read_b128 v[214:217], v0
	ds_read_b128 v[218:221], v197 offset:2048
	ds_read_b128 v[222:225], v197 offset:6144
	s_waitcnt lgkmcnt(4)
	v_mfma_f32_16x16x32_bf16 v[210:213], v[94:97], v[202:205], v[210:213]
	v_mfma_f32_16x16x32_bf16 v[86:89], v[94:97], v[206:209], v[86:89]
	ds_read_b128 v[94:97], v0 offset:4096
	s_waitcnt lgkmcnt(4)
	v_mfma_f32_16x16x32_bf16 v[78:81], v[198:201], v[202:205], v[78:81]
	ds_read_b128 v[202:205], v0 offset:8192
	v_mfma_f32_16x16x32_bf16 v[82:85], v[198:201], v[206:209], v[82:85]
	s_waitcnt lgkmcnt(3)
	v_mfma_f32_16x16x32_bf16 v[90:93], v[214:217], v[218:221], v[90:93]
	ds_read_b128 v[198:201], v0 offset:12288
	s_waitcnt lgkmcnt(3)
	v_mfma_f32_16x16x32_bf16 v[70:73], v[214:217], v[222:225], v[70:73]
	v_add_u32_e32 v0, s0, v145
	s_waitcnt lgkmcnt(2)
	v_mfma_f32_16x16x32_bf16 v[206:209], v[94:97], v[218:221], v[98:101]
	v_mfma_f32_16x16x32_bf16 v[74:77], v[94:97], v[222:225], v[74:77]
	ds_read_b128 v[94:97], v0
	ds_read_b128 v[214:217], v197 offset:3072
	ds_read_b128 v[228:231], v197 offset:7168
	s_waitcnt lgkmcnt(4)
	v_mfma_f32_16x16x32_bf16 v[210:213], v[202:205], v[218:221], v[210:213]
	v_mfma_f32_16x16x32_bf16 v[86:89], v[202:205], v[222:225], v[86:89]
	ds_read_b128 v[202:205], v0 offset:4096
	ds_read_b128 v[232:235], v0 offset:8192
	s_waitcnt lgkmcnt(5)
	v_mfma_f32_16x16x32_bf16 v[218:221], v[198:201], v[218:221], v[78:81]
	v_mfma_f32_16x16x32_bf16 v[198:201], v[198:201], v[222:225], v[82:85]
	s_waitcnt lgkmcnt(3)
	v_mfma_f32_16x16x32_bf16 v[82:85], v[94:97], v[214:217], v[90:93]
	ds_read_b128 v[222:225], v0 offset:12288
	s_waitcnt lgkmcnt(3)
	v_mfma_f32_16x16x32_bf16 v[98:101], v[94:97], v[228:231], v[70:73]
	s_waitcnt lgkmcnt(2)
	v_mfma_f32_16x16x32_bf16 v[78:81], v[202:205], v[214:217], v[206:209]
	v_mfma_f32_16x16x32_bf16 v[94:97], v[202:205], v[228:231], v[74:77]
	s_waitcnt lgkmcnt(1)
	v_mfma_f32_16x16x32_bf16 v[74:77], v[232:235], v[214:217], v[210:213]
	v_mfma_f32_16x16x32_bf16 v[90:93], v[232:235], v[228:231], v[86:89]
	s_nop 0
	v_max_f32_e32 v0, v82, v83
	s_waitcnt lgkmcnt(0)
	v_mfma_f32_16x16x32_bf16 v[70:73], v[222:225], v[214:217], v[218:221]
	v_max_f32_e32 v2, v84, v85
	s_nop 0
	v_max_f32_e32 v5, v80, v81
	v_max3_f32 v5, v78, v79, v5
	v_max3_f32 v0, v0, v2, v5
	v_max_f32_e32 v2, v76, v77
	s_nop 1
	v_max_f32_e32 v5, v72, v73
	v_max3_f32 v2, v74, v75, v2
	v_max3_f32 v5, v70, v71, v5
	v_max3_f32 v0, v0, v2, v5
	v_mov_b32_e32 v2, v0
	s_nop 1
	v_permlane16_swap_b32_e32 v0, v2
	ds_read_b32 v125, v196 offset:508
	v_max_f32_e32 v0, v0, v2
	v_mov_b32_e32 v2, v0
	s_nop 1
	v_permlane32_swap_b32_e32 v0, v2
	v_max_f32_e32 v0, v0, v2
	s_waitcnt lgkmcnt(0)
	v_fmamk_f32 v0, v0, 0x3fb8aa3b, v125
	v_max_f32_e32 v133, v137, v0
	v_sub_f32_e32 v0, v137, v133
	v_exp_f32_e32 v2, v0
	v_mfma_f32_16x16x32_bf16 v[86:89], v[222:225], v[228:231], v[198:201]
	v_cmp_neq_f32_e32 vcc, 1.0, v2
	s_cbranch_vccz .LBB0_803
	v_pk_mul_f32 v[68:69], v[68:69], v[2:3] op_sel_hi:[1,0]
	v_pk_mul_f32 v[66:67], v[66:67], v[2:3] op_sel_hi:[1,0]
	v_pk_mul_f32 v[64:65], v[64:65], v[2:3] op_sel_hi:[1,0]
	v_pk_mul_f32 v[62:63], v[62:63], v[2:3] op_sel_hi:[1,0]
	v_pk_mul_f32 v[60:61], v[60:61], v[2:3] op_sel_hi:[1,0]
	v_pk_mul_f32 v[58:59], v[58:59], v[2:3] op_sel_hi:[1,0]
	v_pk_mul_f32 v[56:57], v[56:57], v[2:3] op_sel_hi:[1,0]
	v_pk_mul_f32 v[54:55], v[54:55], v[2:3] op_sel_hi:[1,0]
	v_pk_mul_f32 v[52:53], v[52:53], v[2:3] op_sel_hi:[1,0]
	v_pk_mul_f32 v[50:51], v[50:51], v[2:3] op_sel_hi:[1,0]
	v_pk_mul_f32 v[48:49], v[48:49], v[2:3] op_sel_hi:[1,0]
	v_pk_mul_f32 v[46:47], v[46:47], v[2:3] op_sel_hi:[1,0]
	v_pk_mul_f32 v[44:45], v[44:45], v[2:3] op_sel_hi:[1,0]
	v_pk_mul_f32 v[42:43], v[42:43], v[2:3] op_sel_hi:[1,0]
	v_pk_mul_f32 v[40:41], v[40:41], v[2:3] op_sel_hi:[1,0]
	v_pk_mul_f32 v[38:39], v[38:39], v[2:3] op_sel_hi:[1,0]

.LBB0_805:
	v_sub_f32_e32 v0, v125, v134
	v_fmamk_f32 v5, v98, 0x3fb8aa3b, v0
	v_exp_f32_e32 v98, v5
	v_fmamk_f32 v5, v99, 0x3fb8aa3b, v0
	v_exp_f32_e32 v99, v5
	v_fmamk_f32 v5, v100, 0x3fb8aa3b, v0
	v_exp_f32_e32 v100, v5
	v_fmamk_f32 v5, v101, 0x3fb8aa3b, v0
	v_exp_f32_e32 v101, v5
	v_fmamk_f32 v94, v94, 0x3fb8aa3b, v0
	v_add_f32_e32 v5, 0, v98
	v_exp_f32_e32 v94, v94
	v_fmamk_f32 v95, v95, 0x3fb8aa3b, v0
	v_add_f32_e32 v5, v99, v5
	v_exp_f32_e32 v95, v95
	v_fmamk_f32 v96, v96, 0x3fb8aa3b, v0
	v_add_f32_e32 v5, v100, v5
	v_exp_f32_e32 v96, v96
	v_fmamk_f32 v97, v97, 0x3fb8aa3b, v0
	v_add_f32_e32 v5, v101, v5
	v_exp_f32_e32 v97, v97
	v_fmamk_f32 v90, v90, 0x3fb8aa3b, v0
	v_add_f32_e32 v5, v94, v5
	v_exp_f32_e32 v90, v90
	v_fmamk_f32 v91, v91, 0x3fb8aa3b, v0
	v_add_f32_e32 v5, v95, v5
	v_exp_f32_e32 v91, v91
	v_fmamk_f32 v92, v92, 0x3fb8aa3b, v0
	v_add_f32_e32 v5, v96, v5
	v_exp_f32_e32 v92, v92
	v_fmamk_f32 v93, v93, 0x3fb8aa3b, v0
	v_add_f32_e32 v5, v97, v5
	v_exp_f32_e32 v93, v93
	v_fmamk_f32 v86, v86, 0x3fb8aa3b, v0
	v_add_f32_e32 v5, v90, v5
	v_exp_f32_e32 v137, v86
	v_fmamk_f32 v86, v87, 0x3fb8aa3b, v0
	v_add_f32_e32 v5, v91, v5
	v_exp_f32_e32 v198, v86
	v_fmamk_f32 v86, v88, 0x3fb8aa3b, v0
	v_add_f32_e32 v5, v92, v5
	v_exp_f32_e32 v199, v86
	v_fmac_f32_e32 v0, 0x3fb8aa3b, v89
	v_add_f32_e32 v5, v93, v5
	v_exp_f32_e32 v0, v0
	v_add_f32_e32 v5, v137, v5
	v_add_f32_e32 v5, v198, v5
	v_add_f32_e32 v5, v199, v5
	v_add_f32_e32 v5, v0, v5
	v_fmac_f32_e32 v5, v136, v4
	v_sub_f32_e32 v4, v125, v133
	v_fmamk_f32 v82, v82, 0x3fb8aa3b, v4
	v_exp_f32_e32 v82, v82
	v_fmamk_f32 v83, v83, 0x3fb8aa3b, v4
	v_exp_f32_e32 v83, v83
	v_fmamk_f32 v84, v84, 0x3fb8aa3b, v4
	v_exp_f32_e32 v84, v84
	v_fmamk_f32 v85, v85, 0x3fb8aa3b, v4
	v_exp_f32_e32 v85, v85
	v_fmamk_f32 v78, v78, 0x3fb8aa3b, v4
	v_add_f32_e32 v86, 0, v82
	v_exp_f32_e32 v87, v78
	v_fmamk_f32 v78, v79, 0x3fb8aa3b, v4
	v_add_f32_e32 v86, v83, v86
	v_exp_f32_e32 v88, v78
	v_fmamk_f32 v78, v80, 0x3fb8aa3b, v4
	v_add_f32_e32 v86, v84, v86
	v_exp_f32_e32 v89, v78
	v_fmamk_f32 v78, v81, 0x3fb8aa3b, v4
	v_add_f32_e32 v86, v85, v86
	v_exp_f32_e32 v81, v78
	v_fmamk_f32 v74, v74, 0x3fb8aa3b, v4
	v_add_f32_e32 v78, v87, v86
	v_exp_f32_e32 v136, v74
	v_fmamk_f32 v74, v75, 0x3fb8aa3b, v4
	v_add_f32_e32 v78, v88, v78
	v_exp_f32_e32 v200, v74
	v_fmamk_f32 v74, v76, 0x3fb8aa3b, v4
	v_add_f32_e32 v78, v89, v78
	v_exp_f32_e32 v201, v74
	v_fmamk_f32 v74, v77, 0x3fb8aa3b, v4
	v_add_f32_e32 v78, v81, v78
	v_exp_f32_e32 v202, v74
	v_fmamk_f32 v70, v70, 0x3fb8aa3b, v4
	v_add_f32_e32 v74, v136, v78
	v_exp_f32_e32 v203, v70
	v_fmamk_f32 v70, v71, 0x3fb8aa3b, v4
	v_add_f32_e32 v74, v200, v74
	v_exp_f32_e32 v204, v70
	v_fmamk_f32 v70, v72, 0x3fb8aa3b, v4
	v_add_f32_e32 v74, v201, v74
	v_exp_f32_e32 v205, v70
	v_fmac_f32_e32 v4, 0x3fb8aa3b, v73
	v_add_f32_e32 v74, v202, v74
	v_exp_f32_e32 v4, v4
	v_add_f32_e32 v70, v203, v74
	s_cmp_eq_u32 s81, 0
	v_add_f32_e32 v70, v204, v70
	v_add_f32_e32 v70, v205, v70
	s_cselect_b32 s0, 0x8000, s79
	v_add_f32_e32 v125, v4, v70
	s_add_i32 s0, s0, 0
	v_fmac_f32_e32 v125, v135, v2
	v_add_u32_e32 v2, s0, v142
	ds_read_b128 v[70:73], v2
	ds_read_b128 v[74:77], v2 offset:2048
	v_cvt_pk_bf16_f32 v78, v82, v83
	v_cvt_pk_bf16_f32 v79, v84, v85
	ds_read_b128 v[82:85], v2 offset:4096
	v_cvt_pk_bf16_f32 v80, v87, v88
	v_cvt_pk_bf16_f32 v81, v89, v81
	v_cvt_pk_bf16_f32 v86, v98, v99
	v_cvt_pk_bf16_f32 v87, v100, v101
	v_cvt_pk_bf16_f32 v88, v94, v95
	v_cvt_pk_bf16_f32 v89, v96, v97
	s_waitcnt lgkmcnt(2)
	v_mfma_f32_16x16x32_bf16 v[66:69], v[70:73], v[78:81], v[66:69]
	v_mfma_f32_16x16x32_bf16 v[34:37], v[70:73], v[86:89], v[34:37]
	ds_read_b128 v[70:73], v2 offset:6144
	s_waitcnt lgkmcnt(2)
	v_mfma_f32_16x16x32_bf16 v[62:65], v[74:77], v[78:81], v[62:65]
	v_mfma_f32_16x16x32_bf16 v[30:33], v[74:77], v[86:89], v[30:33]
	ds_read_b128 v[74:77], v2 offset:8192
	s_waitcnt lgkmcnt(2)
	v_mfma_f32_16x16x32_bf16 v[58:61], v[82:85], v[78:81], v[58:61]
	v_mfma_f32_16x16x32_bf16 v[26:29], v[82:85], v[86:89], v[26:29]
	ds_read_b128 v[82:85], v2 offset:10240
	s_waitcnt lgkmcnt(2)
	v_mfma_f32_16x16x32_bf16 v[54:57], v[70:73], v[78:81], v[54:57]
	v_mfma_f32_16x16x32_bf16 v[22:25], v[70:73], v[86:89], v[22:25]
	ds_read_b128 v[70:73], v2 offset:12288
	s_waitcnt lgkmcnt(2)
	v_mfma_f32_16x16x32_bf16 v[50:53], v[74:77], v[78:81], v[50:53]
	v_mfma_f32_16x16x32_bf16 v[18:21], v[74:77], v[86:89], v[18:21]
	ds_read_b128 v[74:77], v2 offset:14336
	v_add_u32_e32 v2, s0, v146
	s_waitcnt lgkmcnt(2)
	v_mfma_f32_16x16x32_bf16 v[46:49], v[82:85], v[78:81], v[46:49]
	v_mfma_f32_16x16x32_bf16 v[14:17], v[82:85], v[86:89], v[14:17]
	ds_read_b128 v[82:85], v2
	s_waitcnt lgkmcnt(2)
	v_mfma_f32_16x16x32_bf16 v[42:45], v[70:73], v[78:81], v[42:45]
	v_mfma_f32_16x16x32_bf16 v[10:13], v[70:73], v[86:89], v[10:13]
	ds_read_b128 v[70:73], v2 offset:2048
	s_waitcnt lgkmcnt(2)
	v_mfma_f32_16x16x32_bf16 v[38:41], v[74:77], v[78:81], v[38:41]
	v_cvt_pk_bf16_f32 v78, v90, v91
	v_cvt_pk_bf16_f32 v79, v92, v93
	v_cvt_pk_bf16_f32 v80, v137, v198
	v_mfma_f32_16x16x32_bf16 v[6:9], v[74:77], v[86:89], v[6:9]
	ds_read_b128 v[86:89], v2 offset:4096
	v_cvt_pk_bf16_f32 v74, v136, v200
	v_cvt_pk_bf16_f32 v75, v201, v202
	v_cvt_pk_bf16_f32 v76, v203, v204
	v_cvt_pk_bf16_f32 v77, v205, v4
	v_cvt_pk_bf16_f32 v81, v199, v0
	s_nop 0
	s_waitcnt lgkmcnt(2)
	v_mfma_f32_16x16x32_bf16 v[66:69], v[82:85], v[74:77], v[66:69]
	v_mfma_f32_16x16x32_bf16 v[34:37], v[82:85], v[78:81], v[34:37]
	ds_read_b128 v[82:85], v2 offset:6144
	s_waitcnt lgkmcnt(2)
	v_mfma_f32_16x16x32_bf16 v[62:65], v[70:73], v[74:77], v[62:65]
	v_mfma_f32_16x16x32_bf16 v[30:33], v[70:73], v[78:81], v[30:33]
	ds_read_b128 v[70:73], v2 offset:8192
	s_waitcnt lgkmcnt(2)
	v_mfma_f32_16x16x32_bf16 v[58:61], v[86:89], v[74:77], v[58:61]
	v_mfma_f32_16x16x32_bf16 v[26:29], v[86:89], v[78:81], v[26:29]
	ds_read_b128 v[86:89], v2 offset:10240
	s_waitcnt lgkmcnt(2)
	v_mfma_f32_16x16x32_bf16 v[54:57], v[82:85], v[74:77], v[54:57]
	v_mfma_f32_16x16x32_bf16 v[22:25], v[82:85], v[78:81], v[22:25]
	ds_read_b128 v[82:85], v2 offset:12288
	s_waitcnt lgkmcnt(2)
	v_mfma_f32_16x16x32_bf16 v[50:53], v[70:73], v[74:77], v[50:53]
	v_mfma_f32_16x16x32_bf16 v[18:21], v[70:73], v[78:81], v[18:21]
	ds_read_b128 v[70:73], v2 offset:14336
	s_waitcnt lgkmcnt(2)
	v_mfma_f32_16x16x32_bf16 v[46:49], v[86:89], v[74:77], v[46:49]
	v_mfma_f32_16x16x32_bf16 v[14:17], v[86:89], v[78:81], v[14:17]
	s_waitcnt lgkmcnt(1)
	v_mfma_f32_16x16x32_bf16 v[42:45], v[82:85], v[74:77], v[42:45]
	v_mfma_f32_16x16x32_bf16 v[10:13], v[82:85], v[78:81], v[10:13]
	s_waitcnt lgkmcnt(0)
	v_mfma_f32_16x16x32_bf16 v[38:41], v[70:73], v[74:77], v[38:41]
	s_waitcnt vmcnt(0)
	s_add_i32 s0, s3, s47
	s_cmp_lg_u32 s0, 0
	v_mfma_f32_16x16x32_bf16 v[6:9], v[70:73], v[78:81], v[6:9]
	s_cbranch_scc0 .Lx791_exit
	s_mov_b32 s32, 0
	v_mov_b32_e32 v136, v5
	v_mov_b32_e32 v135, v125
	v_mov_b32_e32 v137, v133
	v_mov_b32_e32 v4, v134
	s_mov_b32 s22, s47
	s_and_b32 s81, s22, 1
	s_add_i32 s47, s22, 1
	s_cmp_ge_i32 s22, s93
	s_cbranch_scc1 .Lx791_pd

.Lx791_800:
	s_lshl_b32 s22, s23, 13
	s_lshl_b32 s0, s23, 6
	s_ashr_i32 s23, s22, 31
	s_lshl_b64 s[22:23], s[22:23], 1
	s_add_u32 s22, s8, s22
	s_addc_u32 s23, s44, s23
	s_cmp_eq_u32 s81, 0
	s_cselect_b32 s1, 0x4000, 0
	s_cselect_b32 s30, s79, 0x8000
	s_add_i32 s1, s28, s1
	v_lshl_add_u64 v[240:241], s[22:23], 0, v[102:103]
	s_mov_b32 s100, s1
	s_ashr_i32 s1, s0, 31
	s_lshl_b64 s[0:1], s[0:1], 1
	s_add_u32 s0, s45, s0
	v_lshl_add_u64 v[242:243], s[22:23], 0, v[108:109]
	s_addc_u32 s1, s46, s1
	s_add_i32 s22, s28, s30
	v_lshl_add_u64 v[244:245], s[0:1], 0, v[106:107]
	s_mov_b32 s101, s22
	v_lshl_add_u64 v[246:247], s[0:1], 0, v[112:113]
	s_mov_b32 s32, 1
.Lx791_pd:
	s_lshl_b32 s0, s81, 14
	s_add_i32 s0, s0, 0
	v_add_u32_e32 v0, s0, v140
	s_waitcnt vmcnt(0)
	s_barrier
	ds_read_b128 v[70:73], v0
	ds_read_b128 v[74:77], v0 offset:4096
	ds_read_b128 v[78:81], v197
	ds_read_b128 v[82:85], v197 offset:4096
	ds_read_b128 v[86:89], v0 offset:8192
	ds_read_b128 v[94:97], v0 offset:12288
	s_cmp_eq_u32 s32, 0
	s_cbranch_scc1 .Lx791_body
	s_mov_b32 m0, s100
	s_nop 0
	global_load_lds_dwordx4 v[240:241], off
	s_add_i32 m0, s100, 0x400
	s_nop 0
	global_load_lds_dwordx4 v[242:243], off
	s_mov_b32 m0, s101
	s_nop 0
	global_load_lds_dwordx4 v[244:245], off
	s_add_i32 m0, s101, 0x400
	s_nop 0
	global_load_lds_dwordx4 v[246:247], off
	s_branch .Lx791_body
.Lx791_exit:
	s_waitcnt vmcnt(0)
	s_barrier
	s_cmp_gt_i32 s37, s93
	s_cbranch_scc1 .LBB0_517
	s_branch .LBB0_808

.LBB0_808:
	s_sub_i32 s0, s33, s42
	s_sub_i32 s47, s0, s43
	s_add_i32 s23, s37, -1
	s_sub_i32 s81, 0, s42
	s_add_i32 s82, s23, 1
	s_cmp_lt_i32 s82, s42
	s_mov_b64 s[0:1], -1
	s_cbranch_scc1 .LBB0_815
	s_branch .LBB0_810
	s_nop 0
	s_nop 0
	s_nop 0
	s_nop 0
	s_nop 0
	s_nop 0
	s_nop 0
	s_nop 0
	s_nop 0
	s_nop 0
	s_nop 0
	s_nop 0
	s_nop 0
	s_nop 0
	s_nop 0
	s_nop 0
	s_nop 0
